# hook tile decode: kernel-argument pointers read with v_readlane from VGPR lanes filled once at kernel entry instead of one s_load_dwordx2 round trip per tile
# speedup vs baseline: 1.0014x; 1.0001x over previous
; #define LAS __attribute__((address_space(3)))
; __device__ __forceinline__ KA ka_get() { KA p = (KA)__builtin_amdgcn_kernarg_segment_ptr(); asm volatile("" : "+s"(p)); return p; }
; #define FRESH() int tid = tid0; asm volatile("" : "+v"(tid)); int bid = bid0, G = G0; asm volatile("" : "+s"(bid), "+s"(G)); const int lane = tid & 63, wave = __builtin_amdgcn_readfirstlane(tid >> 6); (void)lane; (void)wave; (void)bid; (void)G
; __global__ void __launch_bounds__(NTHR, 2) mk_fwd(Args args_unused) {
;     extern __shared__ __attribute__((aligned(16))) unsigned char lds_raw[];
;     LAS unsigned char* lds = (LAS unsigned char*)lds_raw;
;     const int tid0 = threadIdx.x, bid0 = blockIdx.x, G0 = gridDim.x;
;     ...
;     const int tid = tid0;
;     volatile LAS unsigned* MISC = (volatile LAS unsigned*)(lds + MISC_OFF);
;     for (int u = tid; u < (LDS_BYTES - LDSCTL_OFF) / 4; u += NTHR) ((LAS unsigned*)(lds + LDSCTL_OFF))[u] = 0u;
;     __syncthreads();
;     int lo, hi;
;     XcdBarrier bar;
;     { FRESH(); KA A = ka_get(); lo = A->ph_lo; hi = A->ph_hi; gu32* ctl = (gu32*)(A->ws + WS_CTL);
;       bar.bar = (unsigned*)(ctl + CW_BAR); bar.x = 0; bar.st = nullptr;
;       if (!MK_PER_PHASE) bar = xcd_barrier_post((unsigned*)(ctl + CW_BAR), MISC + 8); }
_Z6mk_fwd4Args:
	s_mov_b64 s[92:93], s[0:1]
	s_load_dwordx4 s[4:7], s[92:93], 0xd0
	s_load_dwordx2 s[8:9], s[92:93], 0xe0
	s_load_dwordx2 s[10:11], s[92:93], 0xf8
	s_waitcnt lgkmcnt(0)
	v_writelane_b32 v255, s4, 32
	v_writelane_b32 v255, s5, 33
	v_writelane_b32 v255, s6, 34
	v_writelane_b32 v255, s7, 35
	v_writelane_b32 v255, s8, 36
	v_writelane_b32 v255, s9, 37
	v_writelane_b32 v255, s10, 38
	v_writelane_b32 v255, s11, 39
	s_load_dword s72, s[92:93], 0x108
	s_add_u32 s0, s92, 0x108
	s_addc_u32 s1, s93, 0
	v_lshl_add_u32 v1, v0, 2, 0
	v_writelane_b32 v252, s0, 0
	v_add_u32_e32 v1, 0x24000, v1
	v_mov_b32_e32 v2, 0
	s_mov_b32 s71, s2
	v_writelane_b32 v252, s1, 1
	ds_write2st64_b32 v1, v2, v2 offset1:8
	ds_write2st64_b32 v1, v2, v2 offset0:16 offset1:24
	v_or_b32_e32 v1, 0x800, v0
	s_mov_b64 s[0:1], -1
	s_and_saveexec_b64 s[4:5], s[0:1]
	v_lshl_add_u32 v3, v1, 2, 0
	v_add_u32_e32 v3, 0x24000, v3
	ds_write_b32 v3, v2
	s_or_b64 exec, exec, s[4:5]
	s_and_saveexec_b64 s[4:5], s[0:1]
	s_add_i32 s0, 0, 0x24000
	v_lshl_add_u32 v1, v1, 2, s0
	v_mov_b32_e32 v2, 0
	ds_write_b32 v1, v2 offset:2048
	s_or_b64 exec, exec, s[4:5]
	v_or_b32_e32 v1, 0xc00, v0
	v_cmp_gt_u32_e64 s[0:1], 7, 6
	v_cmp_gt_u32_e64 s[2:3], 7, 5
	s_and_saveexec_b64 s[4:5], s[2:3]
	v_lshl_add_u32 v2, v1, 2, 0
	v_add_u32_e32 v2, 0x24000, v2
	v_mov_b32_e32 v3, 0
	ds_write_b32 v2, v3
	s_or_b64 exec, exec, s[4:5]
	s_and_saveexec_b64 s[4:5], s[0:1]
	s_add_i32 s0, 0, 0x24000
	v_lshl_add_u32 v1, v1, 2, s0
	v_mov_b32_e32 v2, 0
	ds_write_b32 v1, v2 offset:2048
	s_or_b64 exec, exec, s[4:5]
	v_mov_b32_e32 v1, v0
	s_mov_b32 s0, s71
	s_waitcnt lgkmcnt(0)
	s_mov_b32 s1, s72
	s_barrier
	s_mov_b64 s[0:1], s[92:93]
	s_load_dwordx4 s[76:79], s[0:1], 0xf8
	s_getreg_b32 s2, hwreg(HW_REG_XCC_ID, 0, 4)
	v_cmp_eq_u32_e64 s[74:75], 0, v0
	s_waitcnt lgkmcnt(0)
	s_add_u32 s0, s76, 0x4000
	s_addc_u32 s1, s77, 0
	s_and_b32 s2, s2, 15
	s_and_saveexec_b64 s[4:5], s[74:75]
	s_cbranch_execz .LBB0_11
	s_mov_b64 s[6:7], exec
	v_mbcnt_lo_u32_b32 v1, s6, 0
	v_mbcnt_hi_u32_b32 v1, s7, v1
	v_cmp_eq_u32_e32 vcc, 0, v1
	s_and_b64 s[8:9], exec, vcc
	s_mov_b64 exec, s[8:9]
	s_cbranch_execz .LBB0_11
	s_lshl_b32 s3, s2, 8
	s_bcnt1_i32_b64 s6, s[6:7]
	v_mov_b32_e32 v1, s3
	v_mov_b32_e32 v2, s6
	global_atomic_add v1, v2, s[0:1] offset:1024

; #define CV_LOAD(j, R) do { ConvTile c_; if (CV_VALID(j) && CV_DEC(CV_TILE(j), c_)) conv_load(c_.W, c_.N, c_.k0, c_.n0, wave, lane, R); } while (0)
; __device__ __forceinline__ bool conv_decode_moe(KA A, int t, ConvTile& c) {
;     unsigned char* ws = A->ws; c.f8 = 1; c.K = D; c.N = FFE; t -= 4096;
;     if (t < 14336) { const int hf = t / 7168, r2 = t % 7168, e = r2 / 896, r = r2 % 896, hk = r & 1, q = r >> 1; c.W = (hf ? A->in[I_MWU] : A->in[I_MWG]) + (size_t)e * D * FFE; c.WT = ws + WS_MUP + (size_t)e * 2 * FFE * D; c.k0 = 128 * (q / 28) + 64 * hk; c.n0 = 256 * (q % 28); c.kind = 2 + hf; return true; } t -= 14336;
;     if (t >= 7168) return false;
;     { const int e = t / 896, r = t % 896, hk = r & 1, q = r >> 1; c.W = A->in[I_MWD] + (size_t)e * FFE * D; c.WT = ws + WS_MDN + (size_t)e * D * FFE; c.K = FFE; c.N = D; c.k0 = 128 * (q >> 3) + 64 * hk; c.n0 = 256 * (q & 7); c.kind = 0; return true; }
; }
; template <int NSLOT, bool MOE> __device__ __forceinline__ void conv_burst(const ConvHook& h, int bid, PG8_LAS unsigned char* T_, int tid) {
;     ...
;     const int p0 = (h.t0 >> 1) + bid, p1 = h.t1 >> 1;
;     ...
;     if constexpr (NSLOT == 4) {
;         f32x4 R0[8], R1[8], R2[8], R3[8];
;         CV_LOAD(0, R0); CV_LOAD(1, R1); CV_LOAD(2, R2);
.LBB0_805:
	s_mov_b32 s101, 0xc0e00000
	v_mov_b32_e32 v200, 0x40e00000
	v_mov_b32_e32 v201, 0x3c800000
	s_and_b32 s2, s73, 0x7ffffe00
	s_add_i32 s2, s28, s2
	s_addk_i32 s2, 0x100
	s_add_i32 s100, s2, 0x200
	s_cmp_lt_i32 s100, s60
	s_cselect_b32 s100, 1, 0
	s_cmp_lt_i32 s2, s60
	s_cselect_b64 s[68:69], -1, 0
	s_cmp_ge_i32 s2, s60
	s_cbranch_scc1 .LBB0_821
	s_lshl_b32 s12, s2, 1
	s_or_b32 s13, s12, 1
	s_cmpk_gt_i32 s13, 0x47ff
	s_waitcnt lgkmcnt(0)
	s_mov_b64 s[4:5], -1
	s_cbranch_scc0 .LBB0_809
	s_movk_i32 s24, 0x1c00
	s_mov_b64 s[4:5], 0
	s_cmpk_gt_u32 s12, 0x63ff
	s_mov_b64 s[6:7], 0
	s_cbranch_scc1 .LBB0_809
	s_add_i32 s13, s13, 0xb800
	s_bfe_u32 s6, s13, 0x90007
	s_mulk_i32 s6, 0x2493
	s_lshr_b32 s18, s6, 16
	v_readlane_b32 s6, v255, 36
	v_readlane_b32 s7, v255, 37
	s_mul_i32 s19, s18, 0x380
	s_sub_i32 s13, s13, s19
	s_and_b32 s13, s13, 0xffff
	s_mul_hi_u32 s19, s18, 0x3800000
	s_mul_i32 s18, s18, 0x3800000
	s_waitcnt lgkmcnt(0)
	s_add_u32 s84, s6, s18
	s_addc_u32 s85, s7, s19
	s_lshl_b32 s6, s13, 3
	s_lshl_b32 s7, s13, 6
	s_and_b32 s6, s6, 0x1f80
	s_and_b32 s7, s7, 64
	s_or_b32 s65, s6, s7
	s_lshl_b32 s6, s13, 7
	s_and_b32 s42, s6, 0x700
	s_movk_i32 s24, 0x800
	s_mov_b64 s[6:7], -1
.LBB0_809:
	s_andn2_b64 vcc, exec, s[4:5]
	s_cbranch_vccnz .LBB0_811
	s_add_i32 s4, s12, 0xfffff001
	s_mul_hi_i32 s5, s4, 0x92492493
	s_add_i32 s5, s5, s4
	s_lshr_b32 s6, s5, 31
	s_ashr_i32 s5, s5, 12
	s_add_i32 s5, s5, s6
	s_mulk_i32 s5, 0x1c00
	s_sub_i32 s4, s4, s5
	s_sext_i32_i16 s5, s4
	s_mulk_i32 s5, 0x4925
	s_lshr_b32 s6, s5, 31
	s_ashr_i32 s5, s5, 24
	s_add_i32 s6, s5, s6
	s_mul_i32 s5, s6, 0x380
	s_sub_i32 s7, s4, s5
	s_sext_i32_i16 s13, s7
	s_lshr_b32 s18, s13, 1
	s_addk_i32 s12, 0xc00
	s_cmpk_lt_u32 s12, 0x37ff
	s_cselect_b32 s4, 32, 34
	s_add_i32 s5, s4, 1
	v_readlane_b32 s5, v255, s5
	v_readlane_b32 s4, v255, s4
	s_mul_hi_i32 s12, s6, 0x3800000
	s_mul_i32 s6, s6, 0x3800000
	s_movk_i32 s24, 0x1c00
	s_waitcnt lgkmcnt(0)
	s_add_u32 s84, s4, s6
	s_addc_u32 s85, s5, s12
	s_ashr_i32 s4, s13, 1
	s_mulk_i32 s4, 0x4925
	s_lshr_b32 s5, s4, 31
	s_ashr_i32 s4, s4, 19
	s_add_i32 s4, s4, s5
	s_lshl_b32 s5, s4, 7
	s_mul_i32 s4, s4, 28
	s_lshl_b32 s6, s7, 6
	s_sub_i32 s4, s18, s4
	s_and_b32 s6, s6, 64
	s_sext_i32_i16 s4, s4
	s_or_b32 s65, s5, s6
	s_lshl_b32 s42, s4, 8
	s_mov_b64 s[6:7], -1

; #define CV_LOAD(j, R) do { ConvTile c_; if (CV_VALID(j) && CV_DEC(CV_TILE(j), c_)) conv_load(c_.W, c_.N, c_.k0, c_.n0, wave, lane, R); } while (0)
; #define CV_PROC(j, R) { ConvTile c_; if (!CV_VALID(j) || !CV_DEC(CV_TILE(j), c_)) break; if constexpr (MOE) conv_emit_moe(c_, R, T, tid, wave, lane); else conv_emit(c_, R, T, tid, wave, lane); }
; __device__ __forceinline__ bool conv_decode_moe(KA A, int t, ConvTile& c) {
;     ...
;     if (t >= 7168) return false;
;     { const int e = t / 896, r = t % 896, hk = r & 1, q = r >> 1; c.W = A->in[I_MWD] + (size_t)e * FFE * D; c.WT = ws + WS_MDN + (size_t)e * D * FFE; c.K = FFE; c.N = D; c.k0 = 128 * (q >> 3) + 64 * hk; c.n0 = 256 * (q & 7); c.kind = 0; return true; }
; template <int NSLOT, bool MOE> __device__ __forceinline__ void conv_burst(const ConvHook& h, int bid, PG8_LAS unsigned char* T_, int tid) {
;     ...
;     const int p0 = (h.t0 >> 1) + bid, p1 = h.t1 >> 1;
;     ...
;     if constexpr (NSLOT == 4) {
;         f32x4 R0[8], R1[8], R2[8], R3[8];
;         CV_LOAD(0, R0); CV_LOAD(1, R1); CV_LOAD(2, R2);
;         for (int j = 0;; j += 4) {
;             CV_LOAD(j + 3, R3); CV_PROC(j, R0)
.LBB0_821:
	s_add_i32 s19, s28, s73
	s_cmp_ge_i32 s19, s60
	s_mov_b64 s[6:7], -1
	s_cbranch_scc1 .LBB0_804
	s_waitcnt lgkmcnt(0)
	v_readlane_b32 s4, v255, 38
	v_readlane_b32 s5, v255, 39
	s_add_i32 s18, s21, s75
	s_cmpk_gt_i32 s19, 0x23ff
	s_mov_b64 vcc, -1
	s_cbranch_scc0 .LBB0_825
	s_mov_b32 s12, 16
	s_mov_b64 vcc, 0
	s_cmpk_gt_u32 s18, 0x63ff
	s_mov_b64 s[6:7], 0
	s_cbranch_scc1 .LBB0_825
	s_add_i32 s0, s18, 0xb800
	s_bfe_u32 s1, s0, 0x90007
	s_mulk_i32 s1, 0x2493
	s_lshr_b32 s1, s1, 16
	s_mul_i32 s6, s1, 0x380
	s_sub_i32 s0, s0, s6
	s_and_b32 s0, s0, 0xffff
	s_mul_i32 s1, s1, 0xe00000
	s_waitcnt lgkmcnt(0)
	s_add_u32 s1, s4, s1
	s_addc_u32 s6, s5, 0
	s_add_u32 s40, s1, 0x25000000
	s_addc_u32 s41, s6, 0
	s_lshl_b32 s1, s0, 3
	s_lshl_b32 s6, s0, 6
	s_and_b32 s1, s1, 0x1f80
	s_and_b32 s6, s6, 64
	s_lshl_b32 s0, s0, 7
	s_or_b32 s64, s1, s6
	s_and_b32 s0, s0, 0x700
	s_mov_b32 s1, 0
	s_mov_b32 s12, 56
	s_mov_b64 s[6:7], -1

; #define CV_LOAD(j, R) do { ConvTile c_; if (CV_VALID(j) && CV_DEC(CV_TILE(j), c_)) conv_load(c_.W, c_.N, c_.k0, c_.n0, wave, lane, R); } while (0)
; #define CV_PROC(j, R) { ConvTile c_; if (!CV_VALID(j) || !CV_DEC(CV_TILE(j), c_)) break; if constexpr (MOE) conv_emit_moe(c_, R, T, tid, wave, lane); else conv_emit(c_, R, T, tid, wave, lane); }
; __device__ __forceinline__ bool conv_decode_moe(KA A, int t, ConvTile& c) {
;     unsigned char* ws = A->ws; c.f8 = 1; c.K = D; c.N = FFE; t -= 4096;
;     if (t < 14336) { const int hf = t / 7168, r2 = t % 7168, e = r2 / 896, r = r2 % 896, hk = r & 1, q = r >> 1; c.W = (hf ? A->in[I_MWU] : A->in[I_MWG]) + (size_t)e * D * FFE; c.WT = ws + WS_MUP + (size_t)e * 2 * FFE * D; c.k0 = 128 * (q / 28) + 64 * hk; c.n0 = 256 * (q % 28); c.kind = 2 + hf; return true; } t -= 14336;
;     if (t >= 7168) return false;
;     { const int e = t / 896, r = t % 896, hk = r & 1, q = r >> 1; c.W = A->in[I_MWD] + (size_t)e * FFE * D; c.WT = ws + WS_MDN + (size_t)e * D * FFE; c.K = FFE; c.N = D; c.k0 = 128 * (q >> 3) + 64 * hk; c.n0 = 256 * (q & 7); c.kind = 0; return true; }
; }
; template <int NSLOT, bool MOE> __device__ __forceinline__ void conv_burst(const ConvHook& h, int bid, PG8_LAS unsigned char* T_, int tid) {
;     ...
;         for (int j = 0;; j += 4) {
;             CV_LOAD(j + 3, R3); CV_PROC(j, R0)
.LBB0_840:
	s_add_i32 s6, s19, 0x200
	s_cmp_ge_i32 s6, s60
	s_cbranch_scc1 .LBB0_858
	s_cmpk_gt_i32 s6, 0x23ff
	s_mov_b64 s[6:7], -1
	s_cbranch_scc0 .LBB0_844
	s_add_i32 s26, s18, 0x400
	s_movk_i32 s24, 0x1c00
	s_mov_b64 s[6:7], 0
	s_cmpk_gt_u32 s26, 0x63ff
	s_mov_b64 s[12:13], 0
	s_cbranch_scc1 .LBB0_844
	s_add_i32 s26, s26, 0xb800
	s_bfe_u32 s12, s26, 0x90007
	s_mulk_i32 s12, 0x2493
	s_lshr_b32 s16, s12, 16
	v_readlane_b32 s12, v255, 36
	v_readlane_b32 s13, v255, 37
	s_mul_i32 s24, s16, 0x380
	s_sub_i32 s24, s26, s24
	s_and_b32 s24, s24, 0xffff
	s_mul_hi_u32 s26, s16, 0x3800000
	s_mul_i32 s16, s16, 0x3800000
	s_waitcnt lgkmcnt(0)
	s_add_u32 s88, s12, s16
	s_addc_u32 s89, s13, s26
	s_lshl_b32 s12, s24, 3
	s_lshl_b32 s13, s24, 6
	s_and_b32 s12, s12, 0x1f80
	s_and_b32 s13, s13, 64
	s_or_b32 s43, s12, s13
	s_lshl_b32 s12, s24, 7
	s_and_b32 s16, s12, 0x700
	s_movk_i32 s24, 0x800
	s_mov_b64 s[12:13], -1
.LBB0_844:
	s_andn2_b64 vcc, exec, s[6:7]
	s_cbranch_vccnz .LBB0_846
	s_add_i32 s6, s18, 0xfffff400
	s_mul_hi_i32 s7, s6, 0x92492493
	s_add_i32 s7, s7, s6
	s_lshr_b32 s12, s7, 31
	s_ashr_i32 s7, s7, 12
	s_add_i32 s7, s7, s12
	s_mulk_i32 s7, 0x1c00
	s_sub_i32 s6, s6, s7
	s_sext_i32_i16 s7, s6
	s_mulk_i32 s7, 0x4925
	s_lshr_b32 s12, s7, 31
	s_ashr_i32 s7, s7, 24
	s_add_i32 s12, s7, s12
	s_mul_i32 s7, s12, 0x380
	s_sub_i32 s13, s6, s7
	s_sext_i32_i16 s16, s13
	s_lshr_b32 s26, s16, 1
	s_add_i32 s6, s18, 0xfff
	s_cmpk_lt_u32 s6, 0x37ff
	s_cselect_b32 s6, 32, 34
	s_add_i32 s7, s6, 1
	v_readlane_b32 s7, v255, s7
	v_readlane_b32 s6, v255, s6
	s_mul_hi_i32 s33, s12, 0x3800000
	s_mul_i32 s12, s12, 0x3800000
	s_movk_i32 s24, 0x1c00
	s_waitcnt lgkmcnt(0)
	s_add_u32 s88, s6, s12
	s_addc_u32 s89, s7, s33
	s_ashr_i32 s6, s16, 1
	s_mulk_i32 s6, 0x4925
	s_lshr_b32 s7, s6, 31
	s_ashr_i32 s6, s6, 19
	s_add_i32 s6, s6, s7
	s_lshl_b32 s7, s6, 7
	s_mul_i32 s6, s6, 28
	s_lshl_b32 s12, s13, 6
	s_sub_i32 s6, s26, s6
	s_and_b32 s12, s12, 64
	s_sext_i32_i16 s6, s6
	v_readlane_b32 s33, v254, 20
	s_or_b32 s43, s7, s12
	s_lshl_b32 s16, s6, 8
	s_mov_b64 s[12:13], -1

; #define CV_LOAD(j, R) do { ConvTile c_; if (CV_VALID(j) && CV_DEC(CV_TILE(j), c_)) conv_load(c_.W, c_.N, c_.k0, c_.n0, wave, lane, R); } while (0)
; #define CV_PROC(j, R) { ConvTile c_; if (!CV_VALID(j) || !CV_DEC(CV_TILE(j), c_)) break; if constexpr (MOE) conv_emit_moe(c_, R, T, tid, wave, lane); else conv_emit(c_, R, T, tid, wave, lane); }
; __device__ __forceinline__ bool conv_decode_moe(KA A, int t, ConvTile& c) {
;     unsigned char* ws = A->ws; c.f8 = 1; c.K = D; c.N = FFE; t -= 4096;
;     if (t < 14336) { const int hf = t / 7168, r2 = t % 7168, e = r2 / 896, r = r2 % 896, hk = r & 1, q = r >> 1; c.W = (hf ? A->in[I_MWU] : A->in[I_MWG]) + (size_t)e * D * FFE; c.WT = ws + WS_MUP + (size_t)e * 2 * FFE * D; c.k0 = 128 * (q / 28) + 64 * hk; c.n0 = 256 * (q % 28); c.kind = 2 + hf; return true; } t -= 14336;
;     if (t >= 7168) return false;
;     { const int e = t / 896, r = t % 896, hk = r & 1, q = r >> 1; c.W = A->in[I_MWD] + (size_t)e * FFE * D; c.WT = ws + WS_MDN + (size_t)e * D * FFE; c.K = FFE; c.N = D; c.k0 = 128 * (q >> 3) + 64 * hk; c.n0 = 256 * (q & 7); c.kind = 0; return true; }
; }
; template <int NSLOT, bool MOE> __device__ __forceinline__ void conv_burst(const ConvHook& h, int bid, PG8_LAS unsigned char* T_, int tid) {
;     ...
;             CV_LOAD(j + 4, R0); CV_PROC(j + 1, R1)
;             CV_LOAD(j + 5, R1); CV_PROC(j + 2, R2)
.LBB0_876:
	s_add_i32 s6, s73, 0x280
	s_and_b32 s6, s6, 0x7ffffe00
	s_add_i32 s6, s6, s28
	s_cmp_ge_i32 s6, s60
	s_cbranch_scc1 .LBB0_892
	s_lshl_b32 s26, s6, 1
	s_or_b32 s33, s26, 1
	s_cmpk_gt_i32 s33, 0x47ff
	s_mov_b64 s[6:7], -1
	s_cbranch_scc0 .LBB0_880
	s_movk_i32 s24, 0x1c00
	s_mov_b64 s[6:7], 0
	s_cmpk_gt_u32 s26, 0x63ff
	s_mov_b64 s[12:13], 0
	s_cbranch_scc1 .LBB0_880
	s_add_i32 s33, s33, 0xb800
	s_bfe_u32 s12, s33, 0x90007
	s_mulk_i32 s12, 0x2493
	s_lshr_b32 s24, s12, 16
	v_readlane_b32 s12, v255, 36
	v_readlane_b32 s13, v255, 37
	s_mul_i32 s30, s24, 0x380
	s_sub_i32 s30, s33, s30
	s_and_b32 s33, s30, 0xffff
	s_mul_hi_u32 s30, s24, 0x3800000
	s_mul_i32 s24, s24, 0x3800000
	s_waitcnt lgkmcnt(0)
	s_add_u32 s92, s12, s24
	s_addc_u32 s93, s13, s30
	s_lshl_b32 s12, s33, 3
	s_lshl_b32 s13, s33, 6
	s_and_b32 s12, s12, 0x1f80
	s_and_b32 s13, s13, 64
	s_or_b32 s30, s12, s13
	s_lshl_b32 s12, s33, 7
	s_and_b32 s61, s12, 0x700
	s_movk_i32 s24, 0x800
	s_mov_b64 s[12:13], -1
.LBB0_880:
	s_andn2_b64 vcc, exec, s[6:7]
	s_cbranch_vccnz .LBB0_882
	s_add_i32 s6, s26, 0xfffff001
	s_mul_hi_i32 s7, s6, 0x92492493
	s_add_i32 s7, s7, s6
	s_lshr_b32 s12, s7, 31
	s_ashr_i32 s7, s7, 12
	s_add_i32 s7, s7, s12
	s_mulk_i32 s7, 0x1c00
	s_sub_i32 s6, s6, s7
	s_sext_i32_i16 s7, s6
	s_mulk_i32 s7, 0x4925
	s_lshr_b32 s12, s7, 31
	s_ashr_i32 s7, s7, 24
	s_add_i32 s12, s7, s12
	s_mul_i32 s7, s12, 0x380
	s_sub_i32 s13, s6, s7
	s_sext_i32_i16 s30, s13
	s_lshr_b32 s33, s30, 1
	s_addk_i32 s26, 0xc00
	s_cmpk_lt_u32 s26, 0x37ff
	s_cselect_b32 s6, 32, 34
	s_add_i32 s7, s6, 1
	v_readlane_b32 s7, v255, s7
	v_readlane_b32 s6, v255, s6
	s_mul_hi_i32 s26, s12, 0x3800000
	s_mul_i32 s12, s12, 0x3800000
	s_movk_i32 s24, 0x1c00
	s_waitcnt lgkmcnt(0)
	s_add_u32 s92, s6, s12
	s_addc_u32 s93, s7, s26
	s_ashr_i32 s6, s30, 1
	s_mulk_i32 s6, 0x4925
	s_lshr_b32 s7, s6, 31
	s_ashr_i32 s6, s6, 19
	s_add_i32 s6, s6, s7
	s_lshl_b32 s7, s6, 7
	s_mul_i32 s6, s6, 28
	s_lshl_b32 s12, s13, 6
	s_sub_i32 s6, s33, s6
	s_and_b32 s12, s12, 64
	s_sext_i32_i16 s6, s6
	s_or_b32 s30, s7, s12
	s_lshl_b32 s61, s6, 8
	s_mov_b64 s[12:13], -1

; #define CV_LOAD(j, R) do { ConvTile c_; if (CV_VALID(j) && CV_DEC(CV_TILE(j), c_)) conv_load(c_.W, c_.N, c_.k0, c_.n0, wave, lane, R); } while (0)
; #define CV_PROC(j, R) { ConvTile c_; if (!CV_VALID(j) || !CV_DEC(CV_TILE(j), c_)) break; if constexpr (MOE) conv_emit_moe(c_, R, T, tid, wave, lane); else conv_emit(c_, R, T, tid, wave, lane); }
; __device__ __forceinline__ bool conv_decode_moe(KA A, int t, ConvTile& c) {
;     unsigned char* ws = A->ws; c.f8 = 1; c.K = D; c.N = FFE; t -= 4096;
;     if (t < 14336) { const int hf = t / 7168, r2 = t % 7168, e = r2 / 896, r = r2 % 896, hk = r & 1, q = r >> 1; c.W = (hf ? A->in[I_MWU] : A->in[I_MWG]) + (size_t)e * D * FFE; c.WT = ws + WS_MUP + (size_t)e * 2 * FFE * D; c.k0 = 128 * (q / 28) + 64 * hk; c.n0 = 256 * (q % 28); c.kind = 2 + hf; return true; } t -= 14336;
;     if (t >= 7168) return false;
;     { const int e = t / 896, r = t % 896, hk = r & 1, q = r >> 1; c.W = A->in[I_MWD] + (size_t)e * FFE * D; c.WT = ws + WS_MDN + (size_t)e * D * FFE; c.K = FFE; c.N = D; c.k0 = 128 * (q >> 3) + 64 * hk; c.n0 = 256 * (q & 7); c.kind = 0; return true; }
; }
; template <int NSLOT, bool MOE> __device__ __forceinline__ void conv_burst(const ConvHook& h, int bid, PG8_LAS unsigned char* T_, int tid) {
;     ...
;             CV_LOAD(j + 6, R2); CV_PROC(j + 3, R3)
.LBB0_911:
	s_addk_i32 s19, 0x300
	s_cmp_ge_i32 s19, s60
	s_cbranch_scc1 .LBB0_928
	s_cmpk_gt_i32 s19, 0x23ff
	s_mov_b64 s[6:7], -1
	s_cbranch_scc0 .LBB0_926
	s_add_i32 s19, s18, 0x600
	s_movk_i32 s24, 0x1c00
	s_mov_b64 s[6:7], 0
	s_cmpk_gt_u32 s19, 0x63ff
	s_mov_b64 s[12:13], 0
	v_readlane_b32 s26, v255, 20
	s_cbranch_scc1 .LBB0_915
	s_add_i32 s19, s19, 0xb800
	s_bfe_u32 s10, s19, 0x90007
	s_mulk_i32 s10, 0x2493
	s_lshr_b32 s12, s10, 16
	v_readlane_b32 s10, v255, 36
	v_readlane_b32 s11, v255, 37
	s_mul_i32 s13, s12, 0x380
	s_sub_i32 s13, s19, s13
	s_and_b32 s13, s13, 0xffff
	s_mul_hi_u32 s19, s12, 0x3800000
	s_mul_i32 s12, s12, 0x3800000
	s_waitcnt lgkmcnt(0)
	s_add_u32 s10, s10, s12
	s_addc_u32 s11, s11, s19
	s_lshl_b32 s12, s13, 3
	s_lshl_b32 s19, s13, 6
	s_and_b32 s12, s12, 0x1f80
	s_and_b32 s19, s19, 64
	s_or_b32 s26, s12, s19
	s_lshl_b32 s12, s13, 7
	s_and_b32 s12, s12, 0x700
	v_writelane_b32 v255, s12, 21
	s_movk_i32 s24, 0x800
	s_mov_b64 s[12:13], -1

; #define CV_LOAD(j, R) do { ConvTile c_; if (CV_VALID(j) && CV_DEC(CV_TILE(j), c_)) conv_load(c_.W, c_.N, c_.k0, c_.n0, wave, lane, R); } while (0)
; #define CV_PROC(j, R) { ConvTile c_; if (!CV_VALID(j) || !CV_DEC(CV_TILE(j), c_)) break; if constexpr (MOE) conv_emit_moe(c_, R, T, tid, wave, lane); else conv_emit(c_, R, T, tid, wave, lane); }
; __device__ __forceinline__ bool conv_decode(KA A, int t, ConvTile& c) {
;     ...
;     if (t < 14336) { const int hf = t / 7168, r2 = t % 7168, e = r2 / 896, r = r2 % 896, hk = r & 1, q = r >> 1; c.W = (hf ? A->in[I_MWU] : A->in[I_MWG]) + (size_t)e * D * FFE; c.WT = ws + WS_MUP + (size_t)e * 2 * FFE * D; c.K = D; c.N = FFE; c.k0 = 128 * (q / 28) + 64 * hk; c.n0 = 256 * (q % 28); c.kind = 2 + hf; return true; } t -= 14336;
;     { const int e = t / 896, r = t % 896, hk = r & 1, q = r >> 1; c.W = A->in[I_MWD] + (size_t)e * FFE * D; c.WT = ws + WS_MDN + (size_t)e * D * FFE; c.K = FFE; c.N = D; c.k0 = 128 * (q >> 3) + 64 * hk; c.n0 = 256 * (q & 7); c.kind = 0; return true; }
; template <int NSLOT, bool MOE> __device__ __forceinline__ void conv_burst(const ConvHook& h, int bid, PG8_LAS unsigned char* T_, int tid) {
;     ...
;             CV_LOAD(j + 6, R2); CV_PROC(j + 3, R3)
.LBB0_927:
	s_add_i32 s6, s18, 0xfffff600
	s_mul_hi_i32 s7, s6, 0x92492493
	s_add_i32 s7, s7, s6
	s_lshr_b32 s10, s7, 31
	s_ashr_i32 s7, s7, 12
	s_add_i32 s7, s7, s10
	s_mulk_i32 s7, 0x1c00
	s_sub_i32 s6, s6, s7
	s_sext_i32_i16 s7, s6
	s_mulk_i32 s7, 0x4925
	s_lshr_b32 s10, s7, 31
	s_ashr_i32 s7, s7, 24
	s_add_i32 s10, s7, s10
	s_mul_i32 s7, s10, 0x380
	s_sub_i32 s12, s6, s7
	s_sext_i32_i16 s13, s12
	s_lshr_b32 s19, s13, 1
	s_addk_i32 s18, 0x11ff
	s_cmpk_lt_u32 s18, 0x37ff
	s_cselect_b32 s6, 32, 34
	s_add_i32 s7, s6, 1
	v_readlane_b32 s7, v255, s7
	v_readlane_b32 s6, v255, s6
	s_mul_hi_i32 s11, s10, 0x3800000
	s_mul_i32 s10, s10, 0x3800000
	s_movk_i32 s24, 0x1c00
	s_waitcnt lgkmcnt(0)
	s_add_u32 s10, s6, s10
	s_addc_u32 s11, s7, s11
	s_ashr_i32 s6, s13, 1
	s_mulk_i32 s6, 0x4925
	s_lshr_b32 s7, s6, 31
	s_ashr_i32 s6, s6, 19
	s_add_i32 s6, s6, s7
	s_lshl_b32 s7, s6, 7
	s_lshl_b32 s12, s12, 6
	s_mul_i32 s6, s6, 28
	s_and_b32 s12, s12, 64
	s_sub_i32 s6, s19, s6
	s_or_b32 s7, s7, s12
	s_sext_i32_i16 s6, s6
	v_writelane_b32 v255, s7, 20
	s_lshl_b32 s6, s6, 8
	v_writelane_b32 v255, s6, 21
	s_branch .LBB0_917

; #define CV_LOAD(j, R) do { ConvTile c_; if (CV_VALID(j) && CV_DEC(CV_TILE(j), c_)) conv_load(c_.W, c_.N, c_.k0, c_.n0, wave, lane, R); } while (0)
; __device__ __forceinline__ bool conv_decode_moe(KA A, int t, ConvTile& c) {
;     unsigned char* ws = A->ws; c.f8 = 1; c.K = D; c.N = FFE; t -= 4096;
;     if (t < 14336) { const int hf = t / 7168, r2 = t % 7168, e = r2 / 896, r = r2 % 896, hk = r & 1, q = r >> 1; c.W = (hf ? A->in[I_MWU] : A->in[I_MWG]) + (size_t)e * D * FFE; c.WT = ws + WS_MUP + (size_t)e * 2 * FFE * D; c.k0 = 128 * (q / 28) + 64 * hk; c.n0 = 256 * (q % 28); c.kind = 2 + hf; return true; } t -= 14336;
;     if (t >= 7168) return false;
;     { const int e = t / 896, r = t % 896, hk = r & 1, q = r >> 1; c.W = A->in[I_MWD] + (size_t)e * FFE * D; c.WT = ws + WS_MDN + (size_t)e * D * FFE; c.K = FFE; c.N = D; c.k0 = 128 * (q >> 3) + 64 * hk; c.n0 = 256 * (q & 7); c.kind = 0; return true; }
; }
; template <int NSLOT, bool MOE> __device__ __forceinline__ void conv_burst(const ConvHook& h, int bid, PG8_LAS unsigned char* T_, int tid) {
;     ...
;     const int p0 = (h.t0 >> 1) + bid, p1 = h.t1 >> 1;
;     ...
;     if constexpr (NSLOT == 4) {
;         f32x4 R0[8], R1[8], R2[8], R3[8];
;         CV_LOAD(0, R0); CV_LOAD(1, R1); CV_LOAD(2, R2);
.LBB0_2316:
	s_mov_b32 s101, 0xc0e00000
	v_mov_b32_e32 v200, 0x40e00000
	v_mov_b32_e32 v201, 0x3c800000
	s_and_b32 s2, s19, 0x7ffffe00
	s_add_i32 s2, s74, s2
	s_addk_i32 s2, 0x100
	s_add_i32 s100, s2, 0x200
	s_cmpk_lt_i32 s100, 0x2646
	s_cselect_b32 s100, 1, 0
	s_cmpk_lt_i32 s2, 0x2646
	s_cselect_b64 s[4:5], -1, 0
	s_cmpk_gt_i32 s2, 0x2645
	s_cbranch_scc1 .LBB0_2330
	s_lshl_b32 s18, s2, 1
	s_or_b32 s33, s18, 1
	s_cmpk_gt_i32 s33, 0x47ff
	s_mov_b64 s[12:13], -1
	s_cbranch_scc0 .LBB0_2319
	s_add_i32 s33, s33, 0xb800
	s_bfe_u32 s6, s33, 0x90007
	s_mulk_i32 s6, 0x2493
	s_lshr_b32 s12, s6, 16
	v_readlane_b32 s6, v255, 36
	v_readlane_b32 s7, v255, 37
	s_mul_i32 s13, s12, 0x380
	s_sub_i32 s13, s33, s13
	s_and_b32 s13, s13, 0xffff
	s_mul_hi_u32 s24, s12, 0x3800000
	s_mul_i32 s12, s12, 0x3800000
	s_waitcnt lgkmcnt(0)
	s_add_u32 s6, s6, s12
	s_addc_u32 s7, s7, s24
	s_lshl_b32 s12, s13, 3
	s_lshl_b32 s24, s13, 6
	s_and_b32 s12, s12, 0x1f80
	s_and_b32 s24, s24, 64
	s_or_b32 s24, s12, s24
	s_lshl_b32 s12, s13, 7
	s_and_b32 s26, s12, 0x700
	s_mov_b64 s[12:13], 0
.LBB0_2319:
	s_andn2_b64 vcc, exec, s[12:13]
	s_movk_i32 s12, 0x800
	s_cbranch_vccnz .LBB0_2321
	s_add_i32 s6, s18, 0xfffff001
	s_mul_hi_i32 s7, s6, 0x92492493
	s_add_i32 s7, s7, s6
	s_lshr_b32 s12, s7, 31
	s_ashr_i32 s7, s7, 12
	s_add_i32 s7, s7, s12
	s_mulk_i32 s7, 0x1c00
	s_sub_i32 s6, s6, s7
	s_sext_i32_i16 s7, s6
	s_mulk_i32 s7, 0x4925
	s_lshr_b32 s12, s7, 31
	s_ashr_i32 s7, s7, 24
	s_add_i32 s13, s7, s12
	s_mul_i32 s7, s13, 0x380
	s_sub_i32 s24, s6, s7
	s_sext_i32_i16 s26, s24
	s_lshr_b32 s33, s26, 1
	s_addk_i32 s18, 0xc00
	s_cmpk_lt_u32 s18, 0x37ff
	s_cselect_b32 s6, 32, 34
	s_add_i32 s7, s6, 1
	v_readlane_b32 s7, v255, s7
	v_readlane_b32 s6, v255, s6
	s_mul_hi_i32 s18, s13, 0x3800000
	s_mul_i32 s13, s13, 0x3800000
	s_movk_i32 s12, 0x1c00
	s_waitcnt lgkmcnt(0)
	s_add_u32 s6, s6, s13
	s_addc_u32 s7, s7, s18
	s_ashr_i32 s13, s26, 1
	s_mulk_i32 s13, 0x4925
	s_lshr_b32 s18, s13, 31
	s_ashr_i32 s13, s13, 19
	s_add_i32 s13, s13, s18
	s_lshl_b32 s18, s13, 7
	s_mul_i32 s13, s13, 28
	s_lshl_b32 s24, s24, 6
	s_sub_i32 s13, s33, s13
	s_and_b32 s24, s24, 64
	s_sext_i32_i16 s13, s13
	s_or_b32 s24, s18, s24
	s_lshl_b32 s26, s13, 8

; #define CV_LOAD(j, R) do { ConvTile c_; if (CV_VALID(j) && CV_DEC(CV_TILE(j), c_)) conv_load(c_.W, c_.N, c_.k0, c_.n0, wave, lane, R); } while (0)
; #define CV_PROC(j, R) { ConvTile c_; if (!CV_VALID(j) || !CV_DEC(CV_TILE(j), c_)) break; if constexpr (MOE) conv_emit_moe(c_, R, T, tid, wave, lane); else conv_emit(c_, R, T, tid, wave, lane); }
; __device__ __forceinline__ bool conv_decode_moe(KA A, int t, ConvTile& c) {
;     ...
;     if (t >= 7168) return false;
;     { const int e = t / 896, r = t % 896, hk = r & 1, q = r >> 1; c.W = A->in[I_MWD] + (size_t)e * FFE * D; c.WT = ws + WS_MDN + (size_t)e * D * FFE; c.K = FFE; c.N = D; c.k0 = 128 * (q >> 3) + 64 * hk; c.n0 = 256 * (q & 7); c.kind = 0; return true; }
; template <int NSLOT, bool MOE> __device__ __forceinline__ void conv_burst(const ConvHook& h, int bid, PG8_LAS unsigned char* T_, int tid) {
;     ...
;     const int p0 = (h.t0 >> 1) + bid, p1 = h.t1 >> 1;
;     ...
;     if constexpr (NSLOT == 4) {
;         f32x4 R0[8], R1[8], R2[8], R3[8];
;         CV_LOAD(0, R0); CV_LOAD(1, R1); CV_LOAD(2, R2);
;         for (int j = 0;; j += 4) {
;             CV_LOAD(j + 3, R3); CV_PROC(j, R0)
.LBB0_2330:
	s_add_i32 s18, s27, s19
	s_add_i32 s12, s18, 0x10ca
	s_cmpk_gt_i32 s12, 0x2645
	s_mov_b64 s[6:7], -1
	s_cbranch_scc1 .LBB0_2315
	s_waitcnt lgkmcnt(0)
	v_readlane_b32 s54, v255, 38
	v_readlane_b32 s55, v255, 39
	s_cmpk_gt_i32 s12, 0x23ff
	s_mov_b64 s[12:13], -1
	s_cbranch_scc0 .LBB0_2333
	s_add_i32 s6, s36, 0xa601
	s_bfe_u32 s7, s6, 0x90007
	s_mulk_i32 s7, 0x2493
	s_lshr_b32 s7, s7, 16
	s_mul_i32 s12, s7, 0x380
	s_sub_i32 s6, s6, s12
	s_and_b32 s12, s6, 0xffff
	s_mul_i32 s7, s7, 0xe00000
	s_waitcnt lgkmcnt(0)
	s_add_u32 s6, s54, s7
	s_addc_u32 s7, s55, 0
	s_add_u32 s6, s6, 0x25000000
	s_addc_u32 s7, s7, 0
	s_lshl_b32 s13, s12, 3
	s_lshl_b32 s24, s12, 6
	s_and_b32 s13, s13, 0x1f80
	s_and_b32 s24, s24, 64
	s_lshl_b32 s12, s12, 7
	s_or_b32 s33, s13, s24
	s_and_b32 s24, s12, 0x700
	s_mov_b64 s[12:13], 0

; #define CV_LOAD(j, R) do { ConvTile c_; if (CV_VALID(j) && CV_DEC(CV_TILE(j), c_)) conv_load(c_.W, c_.N, c_.k0, c_.n0, wave, lane, R); } while (0)
; #define CV_PROC(j, R) { ConvTile c_; if (!CV_VALID(j) || !CV_DEC(CV_TILE(j), c_)) break; if constexpr (MOE) conv_emit_moe(c_, R, T, tid, wave, lane); else conv_emit(c_, R, T, tid, wave, lane); }
; __device__ __forceinline__ bool conv_decode_moe(KA A, int t, ConvTile& c) {
;     unsigned char* ws = A->ws; c.f8 = 1; c.K = D; c.N = FFE; t -= 4096;
;     if (t < 14336) { const int hf = t / 7168, r2 = t % 7168, e = r2 / 896, r = r2 % 896, hk = r & 1, q = r >> 1; c.W = (hf ? A->in[I_MWU] : A->in[I_MWG]) + (size_t)e * D * FFE; c.WT = ws + WS_MUP + (size_t)e * 2 * FFE * D; c.k0 = 128 * (q / 28) + 64 * hk; c.n0 = 256 * (q % 28); c.kind = 2 + hf; return true; } t -= 14336;
;     if (t >= 7168) return false;
;     { const int e = t / 896, r = t % 896, hk = r & 1, q = r >> 1; c.W = A->in[I_MWD] + (size_t)e * FFE * D; c.WT = ws + WS_MDN + (size_t)e * D * FFE; c.K = FFE; c.N = D; c.k0 = 128 * (q >> 3) + 64 * hk; c.n0 = 256 * (q & 7); c.kind = 0; return true; }
; }
; template <int NSLOT, bool MOE> __device__ __forceinline__ void conv_burst(const ConvHook& h, int bid, PG8_LAS unsigned char* T_, int tid) {
;     ...
;         for (int j = 0;; j += 4) {
;             CV_LOAD(j + 3, R3); CV_PROC(j, R0)
.LBB0_2352:
	s_cmpk_gt_i32 s6, 0x23ff
	s_mov_b64 s[12:13], -1
	s_cbranch_scc0 .LBB0_2354
	s_add_i32 s12, s36, 0xaa01
	s_bfe_u32 s6, s12, 0x90007
	s_mulk_i32 s6, 0x2493
	s_lshr_b32 s13, s6, 16
	v_readlane_b32 s6, v255, 36
	v_readlane_b32 s7, v255, 37
	s_mul_i32 s24, s13, 0x380
	s_sub_i32 s12, s12, s24
	s_and_b32 s12, s12, 0xffff
	s_mul_hi_u32 s24, s13, 0x3800000
	s_mul_i32 s13, s13, 0x3800000
	s_waitcnt lgkmcnt(0)
	s_add_u32 s6, s6, s13
	s_addc_u32 s7, s7, s24
	s_lshl_b32 s13, s12, 3
	s_lshl_b32 s24, s12, 6
	s_and_b32 s13, s13, 0x1f80
	s_and_b32 s24, s24, 64
	s_lshl_b32 s12, s12, 7
	s_or_b32 s24, s13, s24
	s_and_b32 s33, s12, 0x700
	s_mov_b64 s[12:13], 0
.LBB0_2354:
	s_andn2_b64 vcc, exec, s[12:13]
	s_movk_i32 s26, 0x800
	s_cbranch_vccnz .LBB0_2356
	s_add_i32 s6, s36, 0xffffe201
	s_mul_hi_i32 s7, s6, 0x92492493
	s_add_i32 s7, s7, s6
	s_lshr_b32 s12, s7, 31
	s_ashr_i32 s7, s7, 12
	s_add_i32 s7, s7, s12
	s_mulk_i32 s7, 0x1c00
	s_sub_i32 s6, s6, s7
	s_sext_i32_i16 s7, s6
	s_mulk_i32 s7, 0x4925
	s_lshr_b32 s12, s7, 31
	s_ashr_i32 s7, s7, 24
	s_add_i32 s12, s7, s12
	s_mul_i32 s7, s12, 0x380
	s_sub_i32 s13, s6, s7
	s_sext_i32_i16 s24, s13
	s_lshr_b32 s33, s24, 1
	s_add_i32 s6, s36, 0xfffffe00
	s_cmpk_lt_u32 s6, 0x37ff
	s_cselect_b32 s6, 32, 34
	s_add_i32 s7, s6, 1
	v_readlane_b32 s7, v255, s7
	v_readlane_b32 s6, v255, s6
	s_mul_hi_i32 s37, s12, 0x3800000
	s_mul_i32 s12, s12, 0x3800000
	s_movk_i32 s26, 0x1c00
	s_waitcnt lgkmcnt(0)
	s_add_u32 s6, s6, s12
	s_addc_u32 s7, s7, s37
	s_ashr_i32 s12, s24, 1
	s_mulk_i32 s12, 0x4925
	s_lshr_b32 s24, s12, 31
	s_ashr_i32 s12, s12, 19
	s_add_i32 s12, s12, s24
	s_lshl_b32 s24, s12, 7
	s_mul_i32 s12, s12, 28
	s_lshl_b32 s13, s13, 6
	s_sub_i32 s12, s33, s12
	s_and_b32 s13, s13, 64
	s_sext_i32_i16 s12, s12
	s_or_b32 s24, s24, s13
	s_lshl_b32 s33, s12, 8

; #define CV_LOAD(j, R) do { ConvTile c_; if (CV_VALID(j) && CV_DEC(CV_TILE(j), c_)) conv_load(c_.W, c_.N, c_.k0, c_.n0, wave, lane, R); } while (0)
; #define CV_PROC(j, R) { ConvTile c_; if (!CV_VALID(j) || !CV_DEC(CV_TILE(j), c_)) break; if constexpr (MOE) conv_emit_moe(c_, R, T, tid, wave, lane); else conv_emit(c_, R, T, tid, wave, lane); }
; __device__ __forceinline__ bool conv_decode_moe(KA A, int t, ConvTile& c) {
;     unsigned char* ws = A->ws; c.f8 = 1; c.K = D; c.N = FFE; t -= 4096;
;     if (t < 14336) { const int hf = t / 7168, r2 = t % 7168, e = r2 / 896, r = r2 % 896, hk = r & 1, q = r >> 1; c.W = (hf ? A->in[I_MWU] : A->in[I_MWG]) + (size_t)e * D * FFE; c.WT = ws + WS_MUP + (size_t)e * 2 * FFE * D; c.k0 = 128 * (q / 28) + 64 * hk; c.n0 = 256 * (q % 28); c.kind = 2 + hf; return true; } t -= 14336;
;     if (t >= 7168) return false;
;     { const int e = t / 896, r = t % 896, hk = r & 1, q = r >> 1; c.W = A->in[I_MWD] + (size_t)e * FFE * D; c.WT = ws + WS_MDN + (size_t)e * D * FFE; c.K = FFE; c.N = D; c.k0 = 128 * (q >> 3) + 64 * hk; c.n0 = 256 * (q & 7); c.kind = 0; return true; }
; }
; template <int NSLOT, bool MOE> __device__ __forceinline__ void conv_burst(const ConvHook& h, int bid, PG8_LAS unsigned char* T_, int tid) {
;     ...
;             CV_LOAD(j + 4, R0); CV_PROC(j + 1, R1)
;             CV_LOAD(j + 5, R1); CV_PROC(j + 2, R2)
.LBB0_2381:
	s_add_i32 s6, s19, 0x280
	s_and_b32 s6, s6, 0x7ffffe00
	s_add_i32 s6, s6, s74
	s_cmpk_gt_i32 s6, 0x2645
	s_cbranch_scc1 .LBB0_2395
	s_lshl_b32 s24, s6, 1
	s_or_b32 s37, s24, 1
	s_cmpk_gt_i32 s37, 0x47ff
	s_mov_b64 s[12:13], -1
	s_cbranch_scc0 .LBB0_2384
	s_add_i32 s37, s37, 0xb800
	s_bfe_u32 s6, s37, 0x90007
	s_mulk_i32 s6, 0x2493
	s_lshr_b32 s12, s6, 16
	v_readlane_b32 s6, v255, 36
	v_readlane_b32 s7, v255, 37
	s_mul_i32 s13, s12, 0x380
	s_sub_i32 s13, s37, s13
	s_and_b32 s13, s13, 0xffff
	s_mul_hi_u32 s26, s12, 0x3800000
	s_mul_i32 s12, s12, 0x3800000
	s_waitcnt lgkmcnt(0)
	s_add_u32 s6, s6, s12
	s_addc_u32 s7, s7, s26
	s_lshl_b32 s12, s13, 3
	s_lshl_b32 s26, s13, 6
	s_and_b32 s12, s12, 0x1f80
	s_and_b32 s26, s26, 64
	s_or_b32 s26, s12, s26
	s_lshl_b32 s12, s13, 7
	s_and_b32 s33, s12, 0x700
	s_mov_b64 s[12:13], 0
.LBB0_2384:
	s_andn2_b64 vcc, exec, s[12:13]
	s_movk_i32 s12, 0x800
	s_cbranch_vccnz .LBB0_2386
	s_add_i32 s6, s24, 0xfffff001
	s_mul_hi_i32 s7, s6, 0x92492493
	s_add_i32 s7, s7, s6
	s_lshr_b32 s12, s7, 31
	s_ashr_i32 s7, s7, 12
	s_add_i32 s7, s7, s12
	s_mulk_i32 s7, 0x1c00
	s_sub_i32 s6, s6, s7
	s_sext_i32_i16 s7, s6
	s_mulk_i32 s7, 0x4925
	s_lshr_b32 s12, s7, 31
	s_ashr_i32 s7, s7, 24
	s_add_i32 s13, s7, s12
	s_mul_i32 s7, s13, 0x380
	s_sub_i32 s26, s6, s7
	s_sext_i32_i16 s33, s26
	s_lshr_b32 s37, s33, 1
	s_addk_i32 s24, 0xc00
	s_cmpk_lt_u32 s24, 0x37ff
	s_cselect_b32 s6, 32, 34
	s_add_i32 s7, s6, 1
	v_readlane_b32 s7, v255, s7
	v_readlane_b32 s6, v255, s6
	s_mul_hi_i32 s24, s13, 0x3800000
	s_mul_i32 s13, s13, 0x3800000
	s_movk_i32 s12, 0x1c00
	s_waitcnt lgkmcnt(0)
	s_add_u32 s6, s6, s13
	s_addc_u32 s7, s7, s24
	s_ashr_i32 s13, s33, 1
	s_mulk_i32 s13, 0x4925
	s_lshr_b32 s24, s13, 31
	s_ashr_i32 s13, s13, 19
	s_add_i32 s13, s13, s24
	s_lshl_b32 s24, s13, 7
	s_mul_i32 s13, s13, 28
	s_lshl_b32 s26, s26, 6
	s_sub_i32 s13, s37, s13
	s_and_b32 s26, s26, 64
	s_sext_i32_i16 s13, s13
	s_or_b32 s26, s24, s26
	s_lshl_b32 s33, s13, 8

; #define CV_LOAD(j, R) do { ConvTile c_; if (CV_VALID(j) && CV_DEC(CV_TILE(j), c_)) conv_load(c_.W, c_.N, c_.k0, c_.n0, wave, lane, R); } while (0)
; #define CV_PROC(j, R) { ConvTile c_; if (!CV_VALID(j) || !CV_DEC(CV_TILE(j), c_)) break; if constexpr (MOE) conv_emit_moe(c_, R, T, tid, wave, lane); else conv_emit(c_, R, T, tid, wave, lane); }
; __device__ __forceinline__ bool conv_decode_moe(KA A, int t, ConvTile& c) {
;     unsigned char* ws = A->ws; c.f8 = 1; c.K = D; c.N = FFE; t -= 4096;
;     if (t < 14336) { const int hf = t / 7168, r2 = t % 7168, e = r2 / 896, r = r2 % 896, hk = r & 1, q = r >> 1; c.W = (hf ? A->in[I_MWU] : A->in[I_MWG]) + (size_t)e * D * FFE; c.WT = ws + WS_MUP + (size_t)e * 2 * FFE * D; c.k0 = 128 * (q / 28) + 64 * hk; c.n0 = 256 * (q % 28); c.kind = 2 + hf; return true; } t -= 14336;
;     if (t >= 7168) return false;
;     { const int e = t / 896, r = t % 896, hk = r & 1, q = r >> 1; c.W = A->in[I_MWD] + (size_t)e * FFE * D; c.WT = ws + WS_MDN + (size_t)e * D * FFE; c.K = FFE; c.N = D; c.k0 = 128 * (q >> 3) + 64 * hk; c.n0 = 256 * (q & 7); c.kind = 0; return true; }
; }
; template <int NSLOT, bool MOE> __device__ __forceinline__ void conv_burst(const ConvHook& h, int bid, PG8_LAS unsigned char* T_, int tid) {
;     ...
;             CV_LOAD(j + 6, R2); CV_PROC(j + 3, R3)
.LBB0_2413:
	s_addk_i32 s18, 0x13ca
	s_cmpk_gt_i32 s18, 0x2645
	v_readlane_b32 s33, v254, 20
	s_cbranch_scc1 .LBB0_2427
	s_cmpk_gt_i32 s18, 0x23ff
	s_mov_b64 s[12:13], -1
	s_cbranch_scc0 .LBB0_2416
	s_add_i32 s12, s36, 0xac01
	s_bfe_u32 s6, s12, 0x90007
	s_mulk_i32 s6, 0x2493
	s_lshr_b32 s13, s6, 16
	v_readlane_b32 s6, v255, 36
	v_readlane_b32 s7, v255, 37
	s_mul_i32 s18, s13, 0x380
	s_sub_i32 s12, s12, s18
	s_and_b32 s12, s12, 0xffff
	s_mul_hi_u32 s18, s13, 0x3800000
	s_mul_i32 s13, s13, 0x3800000
	s_waitcnt lgkmcnt(0)
	s_add_u32 s6, s6, s13
	s_addc_u32 s7, s7, s18
	s_lshl_b32 s13, s12, 3
	s_lshl_b32 s18, s12, 6
	s_and_b32 s13, s13, 0x1f80
	s_and_b32 s18, s18, 64
	s_lshl_b32 s12, s12, 7
	s_or_b32 s18, s13, s18
	s_and_b32 s24, s12, 0x700
	s_mov_b64 s[12:13], 0
.LBB0_2416:
	s_andn2_b64 vcc, exec, s[12:13]
	s_movk_i32 s12, 0x800
	s_cbranch_vccnz .LBB0_2418
	s_add_i32 s6, s36, 0xffffe401
	s_mul_hi_i32 s7, s6, 0x92492493
	s_add_i32 s7, s7, s6
	s_lshr_b32 s12, s7, 31
	s_ashr_i32 s7, s7, 12
	s_add_i32 s7, s7, s12
	s_mulk_i32 s7, 0x1c00
	s_sub_i32 s6, s6, s7
	s_sext_i32_i16 s7, s6
	s_mulk_i32 s7, 0x4925
	s_lshr_b32 s12, s7, 31
	s_ashr_i32 s7, s7, 24
	s_add_i32 s13, s7, s12
	s_mul_i32 s7, s13, 0x380
	s_sub_i32 s18, s6, s7
	s_sext_i32_i16 s24, s18
	s_lshr_b32 s26, s24, 1
	s_cmpk_lt_u32 s36, 0x37ff
	s_cselect_b32 s6, 32, 34
	s_add_i32 s7, s6, 1
	v_readlane_b32 s7, v255, s7
	v_readlane_b32 s6, v255, s6
	s_mul_hi_i32 s33, s13, 0x3800000
	s_mul_i32 s13, s13, 0x3800000
	s_movk_i32 s12, 0x1c00
	s_waitcnt lgkmcnt(0)
	s_add_u32 s6, s6, s13
	s_addc_u32 s7, s7, s33
	s_ashr_i32 s13, s24, 1
	s_mulk_i32 s13, 0x4925
	s_lshr_b32 s24, s13, 31
	s_ashr_i32 s13, s13, 19
	s_add_i32 s13, s13, s24
	s_lshl_b32 s24, s13, 7
	s_mul_i32 s13, s13, 28
	s_lshl_b32 s18, s18, 6
	s_sub_i32 s13, s26, s13
	s_and_b32 s18, s18, 64
	s_sext_i32_i16 s13, s13
	v_readlane_b32 s33, v254, 20
	s_or_b32 s18, s24, s18
	s_lshl_b32 s24, s13, 8
